# P2 GEMM unit order with row groups of 32 (fewer distinct operand tiles per round chip-wide, less HBM re-fetch beside the expert-weight stream) + gla_pass2 loads batched
# baseline (speedup 1.0000x reference)
.LBB0_192:
	s_add_i32 s5, s18, s10
	s_lshr_b32 s11, s5, 10
	s_lshl_b32 s11, s11, 5
	s_and_b32 s5, s5, 0x3ff
	s_lshr_b32 s20, s5, 5
	s_and_b32 s5, s5, 31
	s_add_i32 s22, s11, s5

.LBB0_212:
	s_ashr_i32 s4, s30, 3
	s_add_i32 s4, s41, s4
	s_lshr_b32 s30, s4, 10
	s_lshl_b32 s30, s30, 5
	s_and_b32 s4, s4, 0x3ff
	s_lshr_b32 s40, s4, 5
	s_and_b32 s4, s4, 31
	s_add_i32 s42, s30, s4
	s_mov_b64 s[44:45], s[18:19]
